# DSA selection pass (pass 2): hand-written loop, 4x unrolled, prefetch 3 tiles ahead with exact vmcnt, compare+carry mask building
# speedup vs baseline: 1.0324x; 1.0127x over previous
.LBB0_552:
	v_readlane_b32 s100, v254, 38
	v_readlane_b32 s101, v254, 39
	v_mov_b32_e32 v77, v4
	s_mov_b32 s13, 0
	s_nop 2
	s_add_i32 s1, s13, 1
	s_min_u32 s1, s1, s12
	s_lshl_b32 s1, s1, 14
	v_add_u32_e32 v78, s1, v77
	global_load_dwordx2 v[80:81], v78, s[100:101]
	global_load_dwordx2 v[82:83], v78, s[100:101] offset:512
	global_load_dwordx2 v[84:85], v78, s[100:101] offset:1024
	global_load_dwordx2 v[86:87], v78, s[100:101] offset:1536
	s_add_i32 s1, s13, 2
	s_min_u32 s1, s1, s12
	s_lshl_b32 s1, s1, 14
	v_add_u32_e32 v78, s1, v77
	global_load_dwordx2 v[88:89], v78, s[100:101]
	global_load_dwordx2 v[90:91], v78, s[100:101] offset:512
	global_load_dwordx2 v[92:93], v78, s[100:101] offset:1024
	global_load_dwordx2 v[94:95], v78, s[100:101] offset:1536
.Lp2_loop_a:
	s_add_i32 s1, s13, 3
	s_min_u32 s1, s1, s12
	s_lshl_b32 s1, s1, 14
	v_add_u32_e32 v78, s1, v77
	global_load_dwordx2 v[96:97], v78, s[100:101]
	global_load_dwordx2 v[98:99], v78, s[100:101] offset:512
	global_load_dwordx2 v[100:101], v78, s[100:101] offset:1024
	global_load_dwordx2 v[102:103], v78, s[100:101] offset:1536
	v_sub_u32_e32 v74, v44, v23
	s_waitcnt vmcnt(15)
	v_cvt_f32_f16_e32 v24, v18
	v_cvt_f32_f16_sdwa v25, v18 dst_sel:DWORD dst_unused:UNUSED_PAD src0_sel:WORD_1
	v_cvt_f32_f16_e32 v26, v19
	v_cvt_f32_f16_sdwa v27, v19 dst_sel:DWORD dst_unused:UNUSED_PAD src0_sel:WORD_1
	v_add_u32_e32 v73, 0x64, v74
	v_med3_i32 v73, v73, 0, 4
	v_lshlrev_b32_e64 v73, v73, 1
	v_add_u32_e32 v73, -1, v73
	v_cmp_le_f32_e64 s[28:29], v0, v27
	v_cmp_le_f32_e64 s[30:31], v20, v27
	v_cmp_le_f32_e64 s[34:35], v0, v26
	v_cmp_le_f32_e64 s[36:37], v20, v26
	v_addc_co_u32_e64 v28, s[0:1], 0, 0, s[28:29]
	v_addc_co_u32_e64 v72, s[0:1], 0, 0, s[30:31]
	v_cmp_le_f32_e64 s[28:29], v0, v25
	v_cmp_le_f32_e64 s[30:31], v20, v25
	v_addc_co_u32_e64 v28, s[0:1], v28, v28, s[34:35]
	v_addc_co_u32_e64 v72, s[0:1], v72, v72, s[36:37]
	v_cmp_le_f32_e64 s[34:35], v0, v24
	v_cmp_le_f32_e64 s[36:37], v20, v24
	v_addc_co_u32_e64 v28, s[0:1], v28, v28, s[28:29]
	v_addc_co_u32_e64 v72, s[0:1], v72, v72, s[30:31]
	s_nop 1
	v_addc_co_u32_e64 v28, s[0:1], v28, v28, s[34:35]
	v_addc_co_u32_e64 v72, s[0:1], v72, v72, s[36:37]
	v_bfi_b32 v72, v28, 0, v72
	v_and_b32_e32 v28, v28, v73
	v_and_b32_e32 v72, v72, v73
	v_lshl_or_b32 v75, v72, 16, v28
	v_lshlrev_b32_e32 v75, v21, v75
	v_mov_b32_e32 v76, v75
	s_nop 1
	v_permlane16_swap_b32_e32 v75, v76
	v_or_b32_e32 v75, v75, v76
	v_mov_b32_e32 v76, v75
	s_nop 1
	v_permlane32_swap_b32_e32 v75, v76
	s_and_saveexec_b64 s[0:1], vcc
	v_or_b32_e32 v75, v75, v76
	v_add_u32_e32 v76, 0x18000, v22
	ds_write_b16 v76, v75
	ds_write_b16_d16_hi v22, v75 offset:32768
	s_or_b64 exec, exec, s[0:1]
	s_waitcnt vmcnt(14)
	v_cvt_f32_f16_e32 v24, v16
	v_cvt_f32_f16_sdwa v25, v16 dst_sel:DWORD dst_unused:UNUSED_PAD src0_sel:WORD_1
	v_cvt_f32_f16_e32 v26, v17
	v_cvt_f32_f16_sdwa v27, v17 dst_sel:DWORD dst_unused:UNUSED_PAD src0_sel:WORD_1
	v_add_u32_e32 v73, 0x44, v74
	v_med3_i32 v73, v73, 0, 4
	v_lshlrev_b32_e64 v73, v73, 1
	v_add_u32_e32 v73, -1, v73
	v_cmp_le_f32_e64 s[28:29], v0, v27
	v_cmp_le_f32_e64 s[30:31], v20, v27
	v_cmp_le_f32_e64 s[34:35], v0, v26
	v_cmp_le_f32_e64 s[36:37], v20, v26
	v_addc_co_u32_e64 v28, s[0:1], 0, 0, s[28:29]
	v_addc_co_u32_e64 v72, s[0:1], 0, 0, s[30:31]
	v_cmp_le_f32_e64 s[28:29], v0, v25
	v_cmp_le_f32_e64 s[30:31], v20, v25
	v_addc_co_u32_e64 v28, s[0:1], v28, v28, s[34:35]
	v_addc_co_u32_e64 v72, s[0:1], v72, v72, s[36:37]
	v_cmp_le_f32_e64 s[34:35], v0, v24
	v_cmp_le_f32_e64 s[36:37], v20, v24
	v_addc_co_u32_e64 v28, s[0:1], v28, v28, s[28:29]
	v_addc_co_u32_e64 v72, s[0:1], v72, v72, s[30:31]
	s_nop 1
	v_addc_co_u32_e64 v28, s[0:1], v28, v28, s[34:35]
	v_addc_co_u32_e64 v72, s[0:1], v72, v72, s[36:37]
	v_bfi_b32 v72, v28, 0, v72
	v_and_b32_e32 v28, v28, v73
	v_and_b32_e32 v72, v72, v73
	v_lshl_or_b32 v75, v72, 16, v28
	v_lshlrev_b32_e32 v75, v21, v75
	v_mov_b32_e32 v76, v75
	s_nop 1
	v_permlane16_swap_b32_e32 v75, v76
	v_or_b32_e32 v75, v75, v76
	v_mov_b32_e32 v76, v75
	s_nop 1
	v_permlane32_swap_b32_e32 v75, v76
	s_and_saveexec_b64 s[0:1], vcc
	v_or_b32_e32 v75, v75, v76
	v_add_u32_e32 v76, 0x18004, v22
	ds_write_b16 v76, v75
	ds_write_b16_d16_hi v22, v75 offset:32772
	s_or_b64 exec, exec, s[0:1]
	s_waitcnt vmcnt(13)
	v_cvt_f32_f16_e32 v24, v14
	v_cvt_f32_f16_sdwa v25, v14 dst_sel:DWORD dst_unused:UNUSED_PAD src0_sel:WORD_1
	v_cvt_f32_f16_e32 v26, v15
	v_cvt_f32_f16_sdwa v27, v15 dst_sel:DWORD dst_unused:UNUSED_PAD src0_sel:WORD_1
	v_add_u32_e32 v73, 36, v74
	v_med3_i32 v73, v73, 0, 4
	v_lshlrev_b32_e64 v73, v73, 1
	v_add_u32_e32 v73, -1, v73
	v_cmp_le_f32_e64 s[28:29], v0, v27
	v_cmp_le_f32_e64 s[30:31], v20, v27
	v_cmp_le_f32_e64 s[34:35], v0, v26
	v_cmp_le_f32_e64 s[36:37], v20, v26
	v_addc_co_u32_e64 v28, s[0:1], 0, 0, s[28:29]
	v_addc_co_u32_e64 v72, s[0:1], 0, 0, s[30:31]
	v_cmp_le_f32_e64 s[28:29], v0, v25
	v_cmp_le_f32_e64 s[30:31], v20, v25
	v_addc_co_u32_e64 v28, s[0:1], v28, v28, s[34:35]
	v_addc_co_u32_e64 v72, s[0:1], v72, v72, s[36:37]
	v_cmp_le_f32_e64 s[34:35], v0, v24
	v_cmp_le_f32_e64 s[36:37], v20, v24
	v_addc_co_u32_e64 v28, s[0:1], v28, v28, s[28:29]
	v_addc_co_u32_e64 v72, s[0:1], v72, v72, s[30:31]
	s_nop 1
	v_addc_co_u32_e64 v28, s[0:1], v28, v28, s[34:35]
	v_addc_co_u32_e64 v72, s[0:1], v72, v72, s[36:37]
	v_bfi_b32 v72, v28, 0, v72
	v_and_b32_e32 v28, v28, v73
	v_and_b32_e32 v72, v72, v73
	v_lshl_or_b32 v75, v72, 16, v28
	v_lshlrev_b32_e32 v75, v21, v75
	v_mov_b32_e32 v76, v75
	s_nop 1
	v_permlane16_swap_b32_e32 v75, v76
	v_or_b32_e32 v75, v75, v76
	v_mov_b32_e32 v76, v75
	s_nop 1
	v_permlane32_swap_b32_e32 v75, v76
	s_and_saveexec_b64 s[0:1], vcc
	v_or_b32_e32 v75, v75, v76
	v_add_u32_e32 v76, 0x18008, v22
	ds_write_b16 v76, v75
	ds_write_b16_d16_hi v22, v75 offset:32776
	s_or_b64 exec, exec, s[0:1]
	s_waitcnt vmcnt(12)
	v_cvt_f32_f16_e32 v24, v12
	v_cvt_f32_f16_sdwa v25, v12 dst_sel:DWORD dst_unused:UNUSED_PAD src0_sel:WORD_1
	v_cvt_f32_f16_e32 v26, v13
	v_cvt_f32_f16_sdwa v27, v13 dst_sel:DWORD dst_unused:UNUSED_PAD src0_sel:WORD_1
	v_add_u32_e32 v73, 4, v74
	v_med3_i32 v73, v73, 0, 4
	v_lshlrev_b32_e64 v73, v73, 1
	v_add_u32_e32 v73, -1, v73
	v_cmp_le_f32_e64 s[28:29], v0, v27
	v_cmp_le_f32_e64 s[30:31], v20, v27
	v_cmp_le_f32_e64 s[34:35], v0, v26
	v_cmp_le_f32_e64 s[36:37], v20, v26
	v_addc_co_u32_e64 v28, s[0:1], 0, 0, s[28:29]
	v_addc_co_u32_e64 v72, s[0:1], 0, 0, s[30:31]
	v_cmp_le_f32_e64 s[28:29], v0, v25
	v_cmp_le_f32_e64 s[30:31], v20, v25
	v_addc_co_u32_e64 v28, s[0:1], v28, v28, s[34:35]
	v_addc_co_u32_e64 v72, s[0:1], v72, v72, s[36:37]
	v_cmp_le_f32_e64 s[34:35], v0, v24
	v_cmp_le_f32_e64 s[36:37], v20, v24
	v_addc_co_u32_e64 v28, s[0:1], v28, v28, s[28:29]
	v_addc_co_u32_e64 v72, s[0:1], v72, v72, s[30:31]
	s_nop 1
	v_addc_co_u32_e64 v28, s[0:1], v28, v28, s[34:35]
	v_addc_co_u32_e64 v72, s[0:1], v72, v72, s[36:37]
	v_bfi_b32 v72, v28, 0, v72
	v_and_b32_e32 v28, v28, v73
	v_and_b32_e32 v72, v72, v73
	v_lshl_or_b32 v75, v72, 16, v28
	v_lshlrev_b32_e32 v75, v21, v75
	v_mov_b32_e32 v76, v75
	s_nop 1
	v_permlane16_swap_b32_e32 v75, v76
	v_or_b32_e32 v75, v75, v76
	v_mov_b32_e32 v76, v75
	s_nop 1
	v_permlane32_swap_b32_e32 v75, v76
	s_and_saveexec_b64 s[0:1], vcc
	v_or_b32_e32 v75, v75, v76
	v_add_u32_e32 v76, 0x1800c, v22
	ds_write_b16 v76, v75
	ds_write_b16_d16_hi v22, v75 offset:32780
	s_or_b64 exec, exec, s[0:1]
	s_add_i32 s13, s13, 1
	v_add_u32_e32 v22, 16, v22
	v_add_u32_e32 v23, 0x80, v23
	s_cmp_eq_u32 s13, s50
	s_cbranch_scc1 .Lp2_exit_a
	s_add_i32 s1, s13, 3
	s_min_u32 s1, s1, s12
	s_lshl_b32 s1, s1, 14
	v_add_u32_e32 v78, s1, v77
	global_load_dwordx2 v[18:19], v78, s[100:101]
	global_load_dwordx2 v[16:17], v78, s[100:101] offset:512
	global_load_dwordx2 v[14:15], v78, s[100:101] offset:1024
	global_load_dwordx2 v[12:13], v78, s[100:101] offset:1536
	v_sub_u32_e32 v74, v44, v23
	s_waitcnt vmcnt(15)
	v_cvt_f32_f16_e32 v24, v80
	v_cvt_f32_f16_sdwa v25, v80 dst_sel:DWORD dst_unused:UNUSED_PAD src0_sel:WORD_1
	v_cvt_f32_f16_e32 v26, v81
	v_cvt_f32_f16_sdwa v27, v81 dst_sel:DWORD dst_unused:UNUSED_PAD src0_sel:WORD_1
	v_add_u32_e32 v73, 0x64, v74
	v_med3_i32 v73, v73, 0, 4
	v_lshlrev_b32_e64 v73, v73, 1
	v_add_u32_e32 v73, -1, v73
	v_cmp_le_f32_e64 s[28:29], v0, v27
	v_cmp_le_f32_e64 s[30:31], v20, v27
	v_cmp_le_f32_e64 s[34:35], v0, v26
	v_cmp_le_f32_e64 s[36:37], v20, v26
	v_addc_co_u32_e64 v28, s[0:1], 0, 0, s[28:29]
	v_addc_co_u32_e64 v72, s[0:1], 0, 0, s[30:31]
	v_cmp_le_f32_e64 s[28:29], v0, v25
	v_cmp_le_f32_e64 s[30:31], v20, v25
	v_addc_co_u32_e64 v28, s[0:1], v28, v28, s[34:35]
	v_addc_co_u32_e64 v72, s[0:1], v72, v72, s[36:37]
	v_cmp_le_f32_e64 s[34:35], v0, v24
	v_cmp_le_f32_e64 s[36:37], v20, v24
	v_addc_co_u32_e64 v28, s[0:1], v28, v28, s[28:29]
	v_addc_co_u32_e64 v72, s[0:1], v72, v72, s[30:31]
	s_nop 1
	v_addc_co_u32_e64 v28, s[0:1], v28, v28, s[34:35]
	v_addc_co_u32_e64 v72, s[0:1], v72, v72, s[36:37]
	v_bfi_b32 v72, v28, 0, v72
	v_and_b32_e32 v28, v28, v73
	v_and_b32_e32 v72, v72, v73
	v_lshl_or_b32 v75, v72, 16, v28
	v_lshlrev_b32_e32 v75, v21, v75
	v_mov_b32_e32 v76, v75
	s_nop 1
	v_permlane16_swap_b32_e32 v75, v76
	v_or_b32_e32 v75, v75, v76
	v_mov_b32_e32 v76, v75
	s_nop 1
	v_permlane32_swap_b32_e32 v75, v76
	s_and_saveexec_b64 s[0:1], vcc
	v_or_b32_e32 v75, v75, v76
	v_add_u32_e32 v76, 0x18000, v22
	ds_write_b16 v76, v75
	ds_write_b16_d16_hi v22, v75 offset:32768
	s_or_b64 exec, exec, s[0:1]
	s_waitcnt vmcnt(14)
	v_cvt_f32_f16_e32 v24, v82
	v_cvt_f32_f16_sdwa v25, v82 dst_sel:DWORD dst_unused:UNUSED_PAD src0_sel:WORD_1
	v_cvt_f32_f16_e32 v26, v83
	v_cvt_f32_f16_sdwa v27, v83 dst_sel:DWORD dst_unused:UNUSED_PAD src0_sel:WORD_1
	v_add_u32_e32 v73, 0x44, v74
	v_med3_i32 v73, v73, 0, 4
	v_lshlrev_b32_e64 v73, v73, 1
	v_add_u32_e32 v73, -1, v73
	v_cmp_le_f32_e64 s[28:29], v0, v27
	v_cmp_le_f32_e64 s[30:31], v20, v27
	v_cmp_le_f32_e64 s[34:35], v0, v26
	v_cmp_le_f32_e64 s[36:37], v20, v26
	v_addc_co_u32_e64 v28, s[0:1], 0, 0, s[28:29]
	v_addc_co_u32_e64 v72, s[0:1], 0, 0, s[30:31]
	v_cmp_le_f32_e64 s[28:29], v0, v25
	v_cmp_le_f32_e64 s[30:31], v20, v25
	v_addc_co_u32_e64 v28, s[0:1], v28, v28, s[34:35]
	v_addc_co_u32_e64 v72, s[0:1], v72, v72, s[36:37]
	v_cmp_le_f32_e64 s[34:35], v0, v24
	v_cmp_le_f32_e64 s[36:37], v20, v24
	v_addc_co_u32_e64 v28, s[0:1], v28, v28, s[28:29]
	v_addc_co_u32_e64 v72, s[0:1], v72, v72, s[30:31]
	s_nop 1
	v_addc_co_u32_e64 v28, s[0:1], v28, v28, s[34:35]
	v_addc_co_u32_e64 v72, s[0:1], v72, v72, s[36:37]
	v_bfi_b32 v72, v28, 0, v72
	v_and_b32_e32 v28, v28, v73
	v_and_b32_e32 v72, v72, v73
	v_lshl_or_b32 v75, v72, 16, v28
	v_lshlrev_b32_e32 v75, v21, v75
	v_mov_b32_e32 v76, v75
	s_nop 1
	v_permlane16_swap_b32_e32 v75, v76
	v_or_b32_e32 v75, v75, v76
	v_mov_b32_e32 v76, v75
	s_nop 1
	v_permlane32_swap_b32_e32 v75, v76
	s_and_saveexec_b64 s[0:1], vcc
	v_or_b32_e32 v75, v75, v76
	v_add_u32_e32 v76, 0x18004, v22
	ds_write_b16 v76, v75
	ds_write_b16_d16_hi v22, v75 offset:32772
	s_or_b64 exec, exec, s[0:1]
	s_waitcnt vmcnt(13)
	v_cvt_f32_f16_e32 v24, v84
	v_cvt_f32_f16_sdwa v25, v84 dst_sel:DWORD dst_unused:UNUSED_PAD src0_sel:WORD_1
	v_cvt_f32_f16_e32 v26, v85
	v_cvt_f32_f16_sdwa v27, v85 dst_sel:DWORD dst_unused:UNUSED_PAD src0_sel:WORD_1
	v_add_u32_e32 v73, 36, v74
	v_med3_i32 v73, v73, 0, 4
	v_lshlrev_b32_e64 v73, v73, 1
	v_add_u32_e32 v73, -1, v73
	v_cmp_le_f32_e64 s[28:29], v0, v27
	v_cmp_le_f32_e64 s[30:31], v20, v27
	v_cmp_le_f32_e64 s[34:35], v0, v26
	v_cmp_le_f32_e64 s[36:37], v20, v26
	v_addc_co_u32_e64 v28, s[0:1], 0, 0, s[28:29]
	v_addc_co_u32_e64 v72, s[0:1], 0, 0, s[30:31]
	v_cmp_le_f32_e64 s[28:29], v0, v25
	v_cmp_le_f32_e64 s[30:31], v20, v25
	v_addc_co_u32_e64 v28, s[0:1], v28, v28, s[34:35]
	v_addc_co_u32_e64 v72, s[0:1], v72, v72, s[36:37]
	v_cmp_le_f32_e64 s[34:35], v0, v24
	v_cmp_le_f32_e64 s[36:37], v20, v24
	v_addc_co_u32_e64 v28, s[0:1], v28, v28, s[28:29]
	v_addc_co_u32_e64 v72, s[0:1], v72, v72, s[30:31]
	s_nop 1
	v_addc_co_u32_e64 v28, s[0:1], v28, v28, s[34:35]
	v_addc_co_u32_e64 v72, s[0:1], v72, v72, s[36:37]
	v_bfi_b32 v72, v28, 0, v72
	v_and_b32_e32 v28, v28, v73
	v_and_b32_e32 v72, v72, v73
	v_lshl_or_b32 v75, v72, 16, v28
	v_lshlrev_b32_e32 v75, v21, v75
	v_mov_b32_e32 v76, v75
	s_nop 1
	v_permlane16_swap_b32_e32 v75, v76
	v_or_b32_e32 v75, v75, v76
	v_mov_b32_e32 v76, v75
	s_nop 1
	v_permlane32_swap_b32_e32 v75, v76
	s_and_saveexec_b64 s[0:1], vcc
	v_or_b32_e32 v75, v75, v76
	v_add_u32_e32 v76, 0x18008, v22
	ds_write_b16 v76, v75
	ds_write_b16_d16_hi v22, v75 offset:32776
	s_or_b64 exec, exec, s[0:1]
	s_waitcnt vmcnt(12)
	v_cvt_f32_f16_e32 v24, v86
	v_cvt_f32_f16_sdwa v25, v86 dst_sel:DWORD dst_unused:UNUSED_PAD src0_sel:WORD_1
	v_cvt_f32_f16_e32 v26, v87
	v_cvt_f32_f16_sdwa v27, v87 dst_sel:DWORD dst_unused:UNUSED_PAD src0_sel:WORD_1
	v_add_u32_e32 v73, 4, v74
	v_med3_i32 v73, v73, 0, 4
	v_lshlrev_b32_e64 v73, v73, 1
	v_add_u32_e32 v73, -1, v73
	v_cmp_le_f32_e64 s[28:29], v0, v27
	v_cmp_le_f32_e64 s[30:31], v20, v27
	v_cmp_le_f32_e64 s[34:35], v0, v26
	v_cmp_le_f32_e64 s[36:37], v20, v26
	v_addc_co_u32_e64 v28, s[0:1], 0, 0, s[28:29]
	v_addc_co_u32_e64 v72, s[0:1], 0, 0, s[30:31]
	v_cmp_le_f32_e64 s[28:29], v0, v25
	v_cmp_le_f32_e64 s[30:31], v20, v25
	v_addc_co_u32_e64 v28, s[0:1], v28, v28, s[34:35]
	v_addc_co_u32_e64 v72, s[0:1], v72, v72, s[36:37]
	v_cmp_le_f32_e64 s[34:35], v0, v24
	v_cmp_le_f32_e64 s[36:37], v20, v24
	v_addc_co_u32_e64 v28, s[0:1], v28, v28, s[28:29]
	v_addc_co_u32_e64 v72, s[0:1], v72, v72, s[30:31]
	s_nop 1
	v_addc_co_u32_e64 v28, s[0:1], v28, v28, s[34:35]
	v_addc_co_u32_e64 v72, s[0:1], v72, v72, s[36:37]
	v_bfi_b32 v72, v28, 0, v72
	v_and_b32_e32 v28, v28, v73
	v_and_b32_e32 v72, v72, v73
	v_lshl_or_b32 v75, v72, 16, v28
	v_lshlrev_b32_e32 v75, v21, v75
	v_mov_b32_e32 v76, v75
	s_nop 1
	v_permlane16_swap_b32_e32 v75, v76
	v_or_b32_e32 v75, v75, v76
	v_mov_b32_e32 v76, v75
	s_nop 1
	v_permlane32_swap_b32_e32 v75, v76
	s_and_saveexec_b64 s[0:1], vcc
	v_or_b32_e32 v75, v75, v76
	v_add_u32_e32 v76, 0x1800c, v22
	ds_write_b16 v76, v75
	ds_write_b16_d16_hi v22, v75 offset:32780
	s_or_b64 exec, exec, s[0:1]
	s_add_i32 s13, s13, 1
	v_add_u32_e32 v22, 16, v22
	v_add_u32_e32 v23, 0x80, v23
	s_cmp_eq_u32 s13, s50
	s_cbranch_scc1 .Lp2_exit_a
	s_add_i32 s1, s13, 3
	s_min_u32 s1, s1, s12
	s_lshl_b32 s1, s1, 14
	v_add_u32_e32 v78, s1, v77
	global_load_dwordx2 v[80:81], v78, s[100:101]
	global_load_dwordx2 v[82:83], v78, s[100:101] offset:512
	global_load_dwordx2 v[84:85], v78, s[100:101] offset:1024
	global_load_dwordx2 v[86:87], v78, s[100:101] offset:1536
	v_sub_u32_e32 v74, v44, v23
	s_waitcnt vmcnt(15)
	v_cvt_f32_f16_e32 v24, v88
	v_cvt_f32_f16_sdwa v25, v88 dst_sel:DWORD dst_unused:UNUSED_PAD src0_sel:WORD_1
	v_cvt_f32_f16_e32 v26, v89
	v_cvt_f32_f16_sdwa v27, v89 dst_sel:DWORD dst_unused:UNUSED_PAD src0_sel:WORD_1
	v_add_u32_e32 v73, 0x64, v74
	v_med3_i32 v73, v73, 0, 4
	v_lshlrev_b32_e64 v73, v73, 1
	v_add_u32_e32 v73, -1, v73
	v_cmp_le_f32_e64 s[28:29], v0, v27
	v_cmp_le_f32_e64 s[30:31], v20, v27
	v_cmp_le_f32_e64 s[34:35], v0, v26
	v_cmp_le_f32_e64 s[36:37], v20, v26
	v_addc_co_u32_e64 v28, s[0:1], 0, 0, s[28:29]
	v_addc_co_u32_e64 v72, s[0:1], 0, 0, s[30:31]
	v_cmp_le_f32_e64 s[28:29], v0, v25
	v_cmp_le_f32_e64 s[30:31], v20, v25
	v_addc_co_u32_e64 v28, s[0:1], v28, v28, s[34:35]
	v_addc_co_u32_e64 v72, s[0:1], v72, v72, s[36:37]
	v_cmp_le_f32_e64 s[34:35], v0, v24
	v_cmp_le_f32_e64 s[36:37], v20, v24
	v_addc_co_u32_e64 v28, s[0:1], v28, v28, s[28:29]
	v_addc_co_u32_e64 v72, s[0:1], v72, v72, s[30:31]
	s_nop 1
	v_addc_co_u32_e64 v28, s[0:1], v28, v28, s[34:35]
	v_addc_co_u32_e64 v72, s[0:1], v72, v72, s[36:37]
	v_bfi_b32 v72, v28, 0, v72
	v_and_b32_e32 v28, v28, v73
	v_and_b32_e32 v72, v72, v73
	v_lshl_or_b32 v75, v72, 16, v28
	v_lshlrev_b32_e32 v75, v21, v75
	v_mov_b32_e32 v76, v75
	s_nop 1
	v_permlane16_swap_b32_e32 v75, v76
	v_or_b32_e32 v75, v75, v76
	v_mov_b32_e32 v76, v75
	s_nop 1
	v_permlane32_swap_b32_e32 v75, v76
	s_and_saveexec_b64 s[0:1], vcc
	v_or_b32_e32 v75, v75, v76
	v_add_u32_e32 v76, 0x18000, v22
	ds_write_b16 v76, v75
	ds_write_b16_d16_hi v22, v75 offset:32768
	s_or_b64 exec, exec, s[0:1]
	s_waitcnt vmcnt(14)
	v_cvt_f32_f16_e32 v24, v90
	v_cvt_f32_f16_sdwa v25, v90 dst_sel:DWORD dst_unused:UNUSED_PAD src0_sel:WORD_1
	v_cvt_f32_f16_e32 v26, v91
	v_cvt_f32_f16_sdwa v27, v91 dst_sel:DWORD dst_unused:UNUSED_PAD src0_sel:WORD_1
	v_add_u32_e32 v73, 0x44, v74
	v_med3_i32 v73, v73, 0, 4
	v_lshlrev_b32_e64 v73, v73, 1
	v_add_u32_e32 v73, -1, v73
	v_cmp_le_f32_e64 s[28:29], v0, v27
	v_cmp_le_f32_e64 s[30:31], v20, v27
	v_cmp_le_f32_e64 s[34:35], v0, v26
	v_cmp_le_f32_e64 s[36:37], v20, v26
	v_addc_co_u32_e64 v28, s[0:1], 0, 0, s[28:29]
	v_addc_co_u32_e64 v72, s[0:1], 0, 0, s[30:31]
	v_cmp_le_f32_e64 s[28:29], v0, v25
	v_cmp_le_f32_e64 s[30:31], v20, v25
	v_addc_co_u32_e64 v28, s[0:1], v28, v28, s[34:35]
	v_addc_co_u32_e64 v72, s[0:1], v72, v72, s[36:37]
	v_cmp_le_f32_e64 s[34:35], v0, v24
	v_cmp_le_f32_e64 s[36:37], v20, v24
	v_addc_co_u32_e64 v28, s[0:1], v28, v28, s[28:29]
	v_addc_co_u32_e64 v72, s[0:1], v72, v72, s[30:31]
	s_nop 1
	v_addc_co_u32_e64 v28, s[0:1], v28, v28, s[34:35]
	v_addc_co_u32_e64 v72, s[0:1], v72, v72, s[36:37]
	v_bfi_b32 v72, v28, 0, v72
	v_and_b32_e32 v28, v28, v73
	v_and_b32_e32 v72, v72, v73
	v_lshl_or_b32 v75, v72, 16, v28
	v_lshlrev_b32_e32 v75, v21, v75
	v_mov_b32_e32 v76, v75
	s_nop 1
	v_permlane16_swap_b32_e32 v75, v76
	v_or_b32_e32 v75, v75, v76
	v_mov_b32_e32 v76, v75
	s_nop 1
	v_permlane32_swap_b32_e32 v75, v76
	s_and_saveexec_b64 s[0:1], vcc
	v_or_b32_e32 v75, v75, v76
	v_add_u32_e32 v76, 0x18004, v22
	ds_write_b16 v76, v75
	ds_write_b16_d16_hi v22, v75 offset:32772
	s_or_b64 exec, exec, s[0:1]
	s_waitcnt vmcnt(13)
	v_cvt_f32_f16_e32 v24, v92
	v_cvt_f32_f16_sdwa v25, v92 dst_sel:DWORD dst_unused:UNUSED_PAD src0_sel:WORD_1
	v_cvt_f32_f16_e32 v26, v93
	v_cvt_f32_f16_sdwa v27, v93 dst_sel:DWORD dst_unused:UNUSED_PAD src0_sel:WORD_1
	v_add_u32_e32 v73, 36, v74
	v_med3_i32 v73, v73, 0, 4
	v_lshlrev_b32_e64 v73, v73, 1
	v_add_u32_e32 v73, -1, v73
	v_cmp_le_f32_e64 s[28:29], v0, v27
	v_cmp_le_f32_e64 s[30:31], v20, v27
	v_cmp_le_f32_e64 s[34:35], v0, v26
	v_cmp_le_f32_e64 s[36:37], v20, v26
	v_addc_co_u32_e64 v28, s[0:1], 0, 0, s[28:29]
	v_addc_co_u32_e64 v72, s[0:1], 0, 0, s[30:31]
	v_cmp_le_f32_e64 s[28:29], v0, v25
	v_cmp_le_f32_e64 s[30:31], v20, v25
	v_addc_co_u32_e64 v28, s[0:1], v28, v28, s[34:35]
	v_addc_co_u32_e64 v72, s[0:1], v72, v72, s[36:37]
	v_cmp_le_f32_e64 s[34:35], v0, v24
	v_cmp_le_f32_e64 s[36:37], v20, v24
	v_addc_co_u32_e64 v28, s[0:1], v28, v28, s[28:29]
	v_addc_co_u32_e64 v72, s[0:1], v72, v72, s[30:31]
	s_nop 1
	v_addc_co_u32_e64 v28, s[0:1], v28, v28, s[34:35]
	v_addc_co_u32_e64 v72, s[0:1], v72, v72, s[36:37]
	v_bfi_b32 v72, v28, 0, v72
	v_and_b32_e32 v28, v28, v73
	v_and_b32_e32 v72, v72, v73
	v_lshl_or_b32 v75, v72, 16, v28
	v_lshlrev_b32_e32 v75, v21, v75
	v_mov_b32_e32 v76, v75
	s_nop 1
	v_permlane16_swap_b32_e32 v75, v76
	v_or_b32_e32 v75, v75, v76
	v_mov_b32_e32 v76, v75
	s_nop 1
	v_permlane32_swap_b32_e32 v75, v76
	s_and_saveexec_b64 s[0:1], vcc
	v_or_b32_e32 v75, v75, v76
	v_add_u32_e32 v76, 0x18008, v22
	ds_write_b16 v76, v75
	ds_write_b16_d16_hi v22, v75 offset:32776
	s_or_b64 exec, exec, s[0:1]
	s_waitcnt vmcnt(12)
	v_cvt_f32_f16_e32 v24, v94
	v_cvt_f32_f16_sdwa v25, v94 dst_sel:DWORD dst_unused:UNUSED_PAD src0_sel:WORD_1
	v_cvt_f32_f16_e32 v26, v95
	v_cvt_f32_f16_sdwa v27, v95 dst_sel:DWORD dst_unused:UNUSED_PAD src0_sel:WORD_1
	v_add_u32_e32 v73, 4, v74
	v_med3_i32 v73, v73, 0, 4
	v_lshlrev_b32_e64 v73, v73, 1
	v_add_u32_e32 v73, -1, v73
	v_cmp_le_f32_e64 s[28:29], v0, v27
	v_cmp_le_f32_e64 s[30:31], v20, v27
	v_cmp_le_f32_e64 s[34:35], v0, v26
	v_cmp_le_f32_e64 s[36:37], v20, v26
	v_addc_co_u32_e64 v28, s[0:1], 0, 0, s[28:29]
	v_addc_co_u32_e64 v72, s[0:1], 0, 0, s[30:31]
	v_cmp_le_f32_e64 s[28:29], v0, v25
	v_cmp_le_f32_e64 s[30:31], v20, v25
	v_addc_co_u32_e64 v28, s[0:1], v28, v28, s[34:35]
	v_addc_co_u32_e64 v72, s[0:1], v72, v72, s[36:37]
	v_cmp_le_f32_e64 s[34:35], v0, v24
	v_cmp_le_f32_e64 s[36:37], v20, v24
	v_addc_co_u32_e64 v28, s[0:1], v28, v28, s[28:29]
	v_addc_co_u32_e64 v72, s[0:1], v72, v72, s[30:31]
	s_nop 1
	v_addc_co_u32_e64 v28, s[0:1], v28, v28, s[34:35]
	v_addc_co_u32_e64 v72, s[0:1], v72, v72, s[36:37]
	v_bfi_b32 v72, v28, 0, v72
	v_and_b32_e32 v28, v28, v73
	v_and_b32_e32 v72, v72, v73
	v_lshl_or_b32 v75, v72, 16, v28
	v_lshlrev_b32_e32 v75, v21, v75
	v_mov_b32_e32 v76, v75
	s_nop 1
	v_permlane16_swap_b32_e32 v75, v76
	v_or_b32_e32 v75, v75, v76
	v_mov_b32_e32 v76, v75
	s_nop 1
	v_permlane32_swap_b32_e32 v75, v76
	s_and_saveexec_b64 s[0:1], vcc
	v_or_b32_e32 v75, v75, v76
	v_add_u32_e32 v76, 0x1800c, v22
	ds_write_b16 v76, v75
	ds_write_b16_d16_hi v22, v75 offset:32780
	s_or_b64 exec, exec, s[0:1]
	s_add_i32 s13, s13, 1
	v_add_u32_e32 v22, 16, v22
	v_add_u32_e32 v23, 0x80, v23
	s_cmp_eq_u32 s13, s50
	s_cbranch_scc1 .Lp2_exit_a
	s_add_i32 s1, s13, 3
	s_min_u32 s1, s1, s12
	s_lshl_b32 s1, s1, 14
	v_add_u32_e32 v78, s1, v77
	global_load_dwordx2 v[88:89], v78, s[100:101]
	global_load_dwordx2 v[90:91], v78, s[100:101] offset:512
	global_load_dwordx2 v[92:93], v78, s[100:101] offset:1024
	global_load_dwordx2 v[94:95], v78, s[100:101] offset:1536
	v_sub_u32_e32 v74, v44, v23
	s_waitcnt vmcnt(15)
	v_cvt_f32_f16_e32 v24, v96
	v_cvt_f32_f16_sdwa v25, v96 dst_sel:DWORD dst_unused:UNUSED_PAD src0_sel:WORD_1
	v_cvt_f32_f16_e32 v26, v97
	v_cvt_f32_f16_sdwa v27, v97 dst_sel:DWORD dst_unused:UNUSED_PAD src0_sel:WORD_1
	v_add_u32_e32 v73, 0x64, v74
	v_med3_i32 v73, v73, 0, 4
	v_lshlrev_b32_e64 v73, v73, 1
	v_add_u32_e32 v73, -1, v73
	v_cmp_le_f32_e64 s[28:29], v0, v27
	v_cmp_le_f32_e64 s[30:31], v20, v27
	v_cmp_le_f32_e64 s[34:35], v0, v26
	v_cmp_le_f32_e64 s[36:37], v20, v26
	v_addc_co_u32_e64 v28, s[0:1], 0, 0, s[28:29]
	v_addc_co_u32_e64 v72, s[0:1], 0, 0, s[30:31]
	v_cmp_le_f32_e64 s[28:29], v0, v25
	v_cmp_le_f32_e64 s[30:31], v20, v25
	v_addc_co_u32_e64 v28, s[0:1], v28, v28, s[34:35]
	v_addc_co_u32_e64 v72, s[0:1], v72, v72, s[36:37]
	v_cmp_le_f32_e64 s[34:35], v0, v24
	v_cmp_le_f32_e64 s[36:37], v20, v24
	v_addc_co_u32_e64 v28, s[0:1], v28, v28, s[28:29]
	v_addc_co_u32_e64 v72, s[0:1], v72, v72, s[30:31]
	s_nop 1
	v_addc_co_u32_e64 v28, s[0:1], v28, v28, s[34:35]
	v_addc_co_u32_e64 v72, s[0:1], v72, v72, s[36:37]
	v_bfi_b32 v72, v28, 0, v72
	v_and_b32_e32 v28, v28, v73
	v_and_b32_e32 v72, v72, v73
	v_lshl_or_b32 v75, v72, 16, v28
	v_lshlrev_b32_e32 v75, v21, v75
	v_mov_b32_e32 v76, v75
	s_nop 1
	v_permlane16_swap_b32_e32 v75, v76
	v_or_b32_e32 v75, v75, v76
	v_mov_b32_e32 v76, v75
	s_nop 1
	v_permlane32_swap_b32_e32 v75, v76
	s_and_saveexec_b64 s[0:1], vcc
	v_or_b32_e32 v75, v75, v76
	v_add_u32_e32 v76, 0x18000, v22
	ds_write_b16 v76, v75
	ds_write_b16_d16_hi v22, v75 offset:32768
	s_or_b64 exec, exec, s[0:1]
	s_waitcnt vmcnt(14)
	v_cvt_f32_f16_e32 v24, v98
	v_cvt_f32_f16_sdwa v25, v98 dst_sel:DWORD dst_unused:UNUSED_PAD src0_sel:WORD_1
	v_cvt_f32_f16_e32 v26, v99
	v_cvt_f32_f16_sdwa v27, v99 dst_sel:DWORD dst_unused:UNUSED_PAD src0_sel:WORD_1
	v_add_u32_e32 v73, 0x44, v74
	v_med3_i32 v73, v73, 0, 4
	v_lshlrev_b32_e64 v73, v73, 1
	v_add_u32_e32 v73, -1, v73
	v_cmp_le_f32_e64 s[28:29], v0, v27
	v_cmp_le_f32_e64 s[30:31], v20, v27
	v_cmp_le_f32_e64 s[34:35], v0, v26
	v_cmp_le_f32_e64 s[36:37], v20, v26
	v_addc_co_u32_e64 v28, s[0:1], 0, 0, s[28:29]
	v_addc_co_u32_e64 v72, s[0:1], 0, 0, s[30:31]
	v_cmp_le_f32_e64 s[28:29], v0, v25
	v_cmp_le_f32_e64 s[30:31], v20, v25
	v_addc_co_u32_e64 v28, s[0:1], v28, v28, s[34:35]
	v_addc_co_u32_e64 v72, s[0:1], v72, v72, s[36:37]
	v_cmp_le_f32_e64 s[34:35], v0, v24
	v_cmp_le_f32_e64 s[36:37], v20, v24
	v_addc_co_u32_e64 v28, s[0:1], v28, v28, s[28:29]
	v_addc_co_u32_e64 v72, s[0:1], v72, v72, s[30:31]
	s_nop 1
	v_addc_co_u32_e64 v28, s[0:1], v28, v28, s[34:35]
	v_addc_co_u32_e64 v72, s[0:1], v72, v72, s[36:37]
	v_bfi_b32 v72, v28, 0, v72
	v_and_b32_e32 v28, v28, v73
	v_and_b32_e32 v72, v72, v73
	v_lshl_or_b32 v75, v72, 16, v28
	v_lshlrev_b32_e32 v75, v21, v75
	v_mov_b32_e32 v76, v75
	s_nop 1
	v_permlane16_swap_b32_e32 v75, v76
	v_or_b32_e32 v75, v75, v76
	v_mov_b32_e32 v76, v75
	s_nop 1
	v_permlane32_swap_b32_e32 v75, v76
	s_and_saveexec_b64 s[0:1], vcc
	v_or_b32_e32 v75, v75, v76
	v_add_u32_e32 v76, 0x18004, v22
	ds_write_b16 v76, v75
	ds_write_b16_d16_hi v22, v75 offset:32772
	s_or_b64 exec, exec, s[0:1]
	s_waitcnt vmcnt(13)
	v_cvt_f32_f16_e32 v24, v100
	v_cvt_f32_f16_sdwa v25, v100 dst_sel:DWORD dst_unused:UNUSED_PAD src0_sel:WORD_1
	v_cvt_f32_f16_e32 v26, v101
	v_cvt_f32_f16_sdwa v27, v101 dst_sel:DWORD dst_unused:UNUSED_PAD src0_sel:WORD_1
	v_add_u32_e32 v73, 36, v74
	v_med3_i32 v73, v73, 0, 4
	v_lshlrev_b32_e64 v73, v73, 1
	v_add_u32_e32 v73, -1, v73
	v_cmp_le_f32_e64 s[28:29], v0, v27
	v_cmp_le_f32_e64 s[30:31], v20, v27
	v_cmp_le_f32_e64 s[34:35], v0, v26
	v_cmp_le_f32_e64 s[36:37], v20, v26
	v_addc_co_u32_e64 v28, s[0:1], 0, 0, s[28:29]
	v_addc_co_u32_e64 v72, s[0:1], 0, 0, s[30:31]
	v_cmp_le_f32_e64 s[28:29], v0, v25
	v_cmp_le_f32_e64 s[30:31], v20, v25
	v_addc_co_u32_e64 v28, s[0:1], v28, v28, s[34:35]
	v_addc_co_u32_e64 v72, s[0:1], v72, v72, s[36:37]
	v_cmp_le_f32_e64 s[34:35], v0, v24
	v_cmp_le_f32_e64 s[36:37], v20, v24
	v_addc_co_u32_e64 v28, s[0:1], v28, v28, s[28:29]
	v_addc_co_u32_e64 v72, s[0:1], v72, v72, s[30:31]
	s_nop 1
	v_addc_co_u32_e64 v28, s[0:1], v28, v28, s[34:35]
	v_addc_co_u32_e64 v72, s[0:1], v72, v72, s[36:37]
	v_bfi_b32 v72, v28, 0, v72
	v_and_b32_e32 v28, v28, v73
	v_and_b32_e32 v72, v72, v73
	v_lshl_or_b32 v75, v72, 16, v28
	v_lshlrev_b32_e32 v75, v21, v75
	v_mov_b32_e32 v76, v75
	s_nop 1
	v_permlane16_swap_b32_e32 v75, v76
	v_or_b32_e32 v75, v75, v76
	v_mov_b32_e32 v76, v75
	s_nop 1
	v_permlane32_swap_b32_e32 v75, v76
	s_and_saveexec_b64 s[0:1], vcc
	v_or_b32_e32 v75, v75, v76
	v_add_u32_e32 v76, 0x18008, v22
	ds_write_b16 v76, v75
	ds_write_b16_d16_hi v22, v75 offset:32776
	s_or_b64 exec, exec, s[0:1]
	s_waitcnt vmcnt(12)
	v_cvt_f32_f16_e32 v24, v102
	v_cvt_f32_f16_sdwa v25, v102 dst_sel:DWORD dst_unused:UNUSED_PAD src0_sel:WORD_1
	v_cvt_f32_f16_e32 v26, v103
	v_cvt_f32_f16_sdwa v27, v103 dst_sel:DWORD dst_unused:UNUSED_PAD src0_sel:WORD_1
	v_add_u32_e32 v73, 4, v74
	v_med3_i32 v73, v73, 0, 4
	v_lshlrev_b32_e64 v73, v73, 1
	v_add_u32_e32 v73, -1, v73
	v_cmp_le_f32_e64 s[28:29], v0, v27
	v_cmp_le_f32_e64 s[30:31], v20, v27
	v_cmp_le_f32_e64 s[34:35], v0, v26
	v_cmp_le_f32_e64 s[36:37], v20, v26
	v_addc_co_u32_e64 v28, s[0:1], 0, 0, s[28:29]
	v_addc_co_u32_e64 v72, s[0:1], 0, 0, s[30:31]
	v_cmp_le_f32_e64 s[28:29], v0, v25
	v_cmp_le_f32_e64 s[30:31], v20, v25
	v_addc_co_u32_e64 v28, s[0:1], v28, v28, s[34:35]
	v_addc_co_u32_e64 v72, s[0:1], v72, v72, s[36:37]
	v_cmp_le_f32_e64 s[34:35], v0, v24
	v_cmp_le_f32_e64 s[36:37], v20, v24
	v_addc_co_u32_e64 v28, s[0:1], v28, v28, s[28:29]
	v_addc_co_u32_e64 v72, s[0:1], v72, v72, s[30:31]
	s_nop 1
	v_addc_co_u32_e64 v28, s[0:1], v28, v28, s[34:35]
	v_addc_co_u32_e64 v72, s[0:1], v72, v72, s[36:37]
	v_bfi_b32 v72, v28, 0, v72
	v_and_b32_e32 v28, v28, v73
	v_and_b32_e32 v72, v72, v73
	v_lshl_or_b32 v75, v72, 16, v28
	v_lshlrev_b32_e32 v75, v21, v75
	v_mov_b32_e32 v76, v75
	s_nop 1
	v_permlane16_swap_b32_e32 v75, v76
	v_or_b32_e32 v75, v75, v76
	v_mov_b32_e32 v76, v75
	s_nop 1
	v_permlane32_swap_b32_e32 v75, v76
	s_and_saveexec_b64 s[0:1], vcc
	v_or_b32_e32 v75, v75, v76
	v_add_u32_e32 v76, 0x1800c, v22
	ds_write_b16 v76, v75
	ds_write_b16_d16_hi v22, v75 offset:32780
	s_or_b64 exec, exec, s[0:1]
	s_add_i32 s13, s13, 1
	v_add_u32_e32 v22, 16, v22
	v_add_u32_e32 v23, 0x80, v23
	s_cmp_eq_u32 s13, s50
	s_cbranch_scc1 .Lp2_exit_a
	s_branch .Lp2_loop_a
.Lp2_exit_a:
	s_waitcnt vmcnt(0)
	s_branch .LBB0_562
